# P12 unit tail: the 16 sub-norm gain loads issued up front into free VGPRs with a single wait (were 8 serialized load-pair/wait/store groups)
# baseline (speedup 1.0000x reference)
; template <int PH>
; __device__ __forceinline__ void mk_body(const Args& a) {
;     ...
;             float ss = 0.f;
; #pragma unroll
;             for (int db = 0; db < 4; ++db)
; #pragma unroll
;                 for (int rg = 0; rg < 16; ++rg) ss += oa[db][rg] * oa[db][rg];
;             ss += __shfl_xor(ss, 32);
;             const float rn = (1.0f / sqrtf(ss * (1.0f / 128.0f) + RMS_EPS)) * (1.0f - LAMBDA_INIT);
;             bf16* orow = mixed + ((size_t)b * S + qb * 256 + wave * 32 + rr) * D + h * 128;
; #pragma unroll
;             for (int db = 0; db < 4; ++db)
; #pragma unroll
;                 for (int gp = 0; gp < 2; ++gp) {
;                     const int d0 = 32 * db + 16 * gp + 4 * hh;
;                     const f32x4 g0 = *(const f32x4*)(a.in[11] + d0), g1 = *(const f32x4*)(a.in[11] + d0 + 8);
.LBB0_2371:
	v_mul_f32_e32 v2, v129, v129
	v_fmac_f32_e32 v2, v128, v128
	v_fmac_f32_e32 v2, v130, v130
	v_fmac_f32_e32 v2, v131, v131
	v_fmac_f32_e32 v2, v132, v132
	v_fmac_f32_e32 v2, v133, v133
	v_fmac_f32_e32 v2, v134, v134
	v_fmac_f32_e32 v2, v135, v135
	v_fmac_f32_e32 v2, v136, v136
	v_fmac_f32_e32 v2, v137, v137
	v_fmac_f32_e32 v2, v138, v138
	v_fmac_f32_e32 v2, v139, v139
	v_fmac_f32_e32 v2, v140, v140
	v_fmac_f32_e32 v2, v141, v141
	v_fmac_f32_e32 v2, v142, v142
	v_fmac_f32_e32 v2, v143, v143
	v_fmac_f32_e32 v2, v112, v112
	v_fmac_f32_e32 v2, v113, v113
	v_fmac_f32_e32 v2, v114, v114
	v_mbcnt_lo_u32_b32 v1, -1, 0
	v_mbcnt_hi_u32_b32 v1, -1, v1
	v_fmac_f32_e32 v2, v115, v115
	v_lshrrev_b32_e32 v3, 1, v1
	v_fmac_f32_e32 v2, v116, v116
	v_and_b32_e32 v144, 16, v3
	v_fmac_f32_e32 v2, v117, v117
	global_load_dwordx4 v[4:7], v144, s[62:63]
	global_load_dwordx4 v[8:11], v144, s[62:63] offset:32
	global_load_dwordx4 v[188:191], v144, s[62:63] offset:64
	global_load_dwordx4 v[192:195], v144, s[62:63] offset:96
	global_load_dwordx4 v[196:199], v144, s[62:63] offset:128
	global_load_dwordx4 v[200:203], v144, s[62:63] offset:160
	global_load_dwordx4 v[204:207], v144, s[62:63] offset:192
	global_load_dwordx4 v[208:211], v144, s[62:63] offset:224
	global_load_dwordx4 v[212:215], v144, s[62:63] offset:256
	global_load_dwordx4 v[216:219], v144, s[62:63] offset:288
	global_load_dwordx4 v[220:223], v144, s[62:63] offset:320
	global_load_dwordx4 v[224:227], v144, s[62:63] offset:352
	global_load_dwordx4 v[228:231], v144, s[62:63] offset:384
	global_load_dwordx4 v[232:235], v144, s[62:63] offset:416
	global_load_dwordx4 v[236:239], v144, s[62:63] offset:448
	global_load_dwordx4 v[240:243], v144, s[62:63] offset:480
	v_fmac_f32_e32 v2, v118, v118
	v_fmac_f32_e32 v2, v119, v119
	v_fmac_f32_e32 v2, v120, v120
	v_fmac_f32_e32 v2, v121, v121
	v_fmac_f32_e32 v2, v122, v122
	v_fmac_f32_e32 v2, v123, v123
	v_fmac_f32_e32 v2, v124, v124
	v_fmac_f32_e32 v2, v125, v125
	v_fmac_f32_e32 v2, v126, v126
	v_fmac_f32_e32 v2, v127, v127
	v_fmac_f32_e32 v2, v96, v96
	v_fmac_f32_e32 v2, v97, v97
	v_fmac_f32_e32 v2, v98, v98
	v_fmac_f32_e32 v2, v99, v99
	v_fmac_f32_e32 v2, v100, v100
	v_fmac_f32_e32 v2, v101, v101
	v_fmac_f32_e32 v2, v102, v102
	v_fmac_f32_e32 v2, v103, v103
	v_fmac_f32_e32 v2, v104, v104
	v_fmac_f32_e32 v2, v105, v105
	v_fmac_f32_e32 v2, v106, v106
	v_fmac_f32_e32 v2, v107, v107
	v_fmac_f32_e32 v2, v108, v108
	v_fmac_f32_e32 v2, v109, v109
	v_fmac_f32_e32 v2, v110, v110
	v_fmac_f32_e32 v2, v111, v111
	v_fmac_f32_e32 v2, v80, v80
	v_fmac_f32_e32 v2, v81, v81
	v_fmac_f32_e32 v2, v82, v82
	v_fmac_f32_e32 v2, v83, v83
	v_fmac_f32_e32 v2, v84, v84
	v_fmac_f32_e32 v2, v85, v85
	v_fmac_f32_e32 v2, v86, v86
	v_fmac_f32_e32 v2, v87, v87
	v_fmac_f32_e32 v2, v88, v88
	v_fmac_f32_e32 v2, v89, v89
	v_fmac_f32_e32 v2, v90, v90
	v_fmac_f32_e32 v2, v91, v91
	v_and_b32_e32 v12, 64, v151
	v_fmac_f32_e32 v2, v92, v92
	v_xor_b32_e32 v3, 32, v151
	v_add_u32_e32 v12, 64, v12
	v_fmac_f32_e32 v2, v93, v93
	v_cmp_lt_i32_e32 vcc, v3, v12
	v_fmac_f32_e32 v2, v94, v94
	v_fmac_f32_e32 v2, v95, v95
	v_cndmask_b32_e32 v3, v151, v3, vcc
	v_lshlrev_b32_e32 v3, 2, v3
	ds_bpermute_b32 v3, v3, v2
	s_mov_b32 s0, 0xf800000
	s_lshl_b32 s34, s89, 1
	v_readlane_b32 s89, v254, 29
	s_waitcnt lgkmcnt(0)
	v_add_f32_e32 v2, v2, v3
	v_fmamk_f32 v2, v2, 0x3c000000, v147
	v_mul_f32_e32 v3, 0x4f800000, v2
	v_cmp_gt_f32_e32 vcc, s0, v2
	s_nop 1
	v_cndmask_b32_e32 v2, v2, v3, vcc
	v_sqrt_f32_e32 v3, v2
	s_nop 0
	v_add_u32_e32 v12, -1, v3
	v_fma_f32 v13, -v12, v3, v2
	v_cmp_ge_f32_e64 s[2:3], 0, v13
	v_add_u32_e32 v13, 1, v3
	s_nop 0
	v_cndmask_b32_e64 v12, v3, v12, s[2:3]
	v_fma_f32 v3, -v13, v3, v2
	v_cmp_lt_f32_e64 s[2:3], 0, v3
	s_nop 1
	v_cndmask_b32_e64 v3, v12, v13, s[2:3]
	v_mul_f32_e32 v12, 0x37800000, v3
	v_cndmask_b32_e32 v3, v3, v12, vcc
	v_cmp_class_f32_e32 vcc, v2, v148
	s_nop 1
	v_cndmask_b32_e32 v2, v3, v2, vcc
	v_div_scale_f32 v3, s[0:1], v2, v2, 1.0
	v_rcp_f32_e32 v12, v3
	s_nop 0
	v_fma_f32 v13, -v3, v12, 1.0
	v_fmac_f32_e32 v12, v13, v12
	v_div_scale_f32 v13, vcc, 1.0, v2, 1.0
	v_mul_f32_e32 v14, v13, v12
	v_fma_f32 v15, -v3, v14, v13
	v_fmac_f32_e32 v14, v15, v12
	v_fma_f32 v3, -v3, v14, v13
	v_div_fmas_f32 v3, v3, v12, v14
	v_div_fixup_f32 v2, v3, v2, 1.0
	v_mul_f32_e32 v12, 0x3f24fd5c, v2
	v_and_or_b32 v2, v1, 31, s91
	v_mul_f32_e32 v1, v128, v12
	s_waitcnt vmcnt(0)
; __device__ __forceinline__ unsigned cvt_pk_bf16(float lo, float hi) { unsigned r; asm volatile("v_cvt_pk_bf16_f32 %0, %1, %2" : "=v"(r) : "v"(lo), "v"(hi)); return r; }
; template <int PH>
; __device__ __forceinline__ void mk_body(const Args& a) {
;     ...
; #pragma unroll
;             for (int db = 0; db < 4; ++db)
; #pragma unroll
;                 for (int gp = 0; gp < 2; ++gp) {
;                     const int d0 = 32 * db + 16 * gp + 4 * hh;
;                     const f32x4 g0 = *(const f32x4*)(a.in[11] + d0), g1 = *(const f32x4*)(a.in[11] + d0 + 8);
;                     u32x2 a_, b_;
;                     a_.x = pg8::cvt_pk_bf16(oa[db][8 * gp + 0] * rn * g0.x, oa[db][8 * gp + 1] * rn * g0.y); a_.y = pg8::cvt_pk_bf16(oa[db][8 * gp + 2] * rn * g0.z, oa[db][8 * gp + 3] * rn * g0.w);
;                     b_.x = pg8::cvt_pk_bf16(oa[db][8 * gp + 4] * rn * g1.x, oa[db][8 * gp + 5] * rn * g1.y); b_.y = pg8::cvt_pk_bf16(oa[db][8 * gp + 6] * rn * g1.z, oa[db][8 * gp + 7] * rn * g1.w);
;                     att::swap_pair(a_, b_);
;                     const u32x4 w = {a_.x, a_.y, b_.x, b_.y};
;                     *(u32x4*)(orow + 32 * db + 16 * gp + 8 * hh) = w;
	v_mul_f32_e32 v1, v4, v1
	v_mul_f32_e32 v4, v129, v12
	v_mul_f32_e32 v4, v5, v4
	v_cvt_pk_bf16_f32 v4, v1, v4
	v_mul_f32_e32 v1, v130, v12
	v_mul_f32_e32 v5, v131, v12
	v_mul_f32_e32 v1, v6, v1
	v_mul_f32_e32 v5, v7, v5
	v_mov_b32_e32 v3, s93
	v_cvt_pk_bf16_f32 v5, v1, v5
	v_mul_f32_e32 v1, v132, v12
	v_mul_f32_e32 v6, v133, v12
	v_lshlrev_b64 v[2:3], 11, v[2:3]
	v_mul_f32_e32 v1, v8, v1
	v_mul_f32_e32 v6, v9, v6
	v_mul_f32_e32 v7, v135, v12
	v_lshl_add_u64 v[2:3], s[40:41], 0, v[2:3]
	v_cvt_pk_bf16_f32 v6, v1, v6
	v_mul_f32_e32 v1, v134, v12
	v_mul_f32_e32 v7, v11, v7
	v_lshl_add_u64 v[2:3], v[2:3], 0, s[34:35]
	v_mul_f32_e32 v1, v10, v1
	v_cvt_pk_bf16_f32 v7, v1, v7
	v_lshl_add_u64 v[2:3], v[2:3], 0, v[144:145]
	v_permlane32_swap_b32_e32 v4, v6
	v_permlane32_swap_b32_e32 v5, v7
	global_store_dwordx4 v[2:3], v[4:7], off
	v_mul_f32_e32 v1, v136, v12
	v_mul_f32_e32 v13, v137, v12
	v_mul_f32_e32 v14, v138, v12
	v_mul_f32_e32 v15, v139, v12
	v_mul_f32_e32 v16, v140, v12
	v_mul_f32_e32 v17, v141, v12
	v_mul_f32_e32 v18, v142, v12
	v_mul_f32_e32 v19, v143, v12
	v_readlane_b32 s91, v254, 28
	v_mul_f32_e32 v1, v1, v188
	v_mul_f32_e32 v4, v13, v189
	v_mul_f32_e32 v5, v14, v190
	v_mul_f32_e32 v6, v15, v191
	v_mul_f32_e32 v7, v16, v192
	v_mul_f32_e32 v8, v17, v193
	v_mul_f32_e32 v9, v18, v194
	v_mul_f32_e32 v10, v19, v195
	v_cvt_pk_bf16_f32 v4, v1, v4
	v_cvt_pk_bf16_f32 v5, v5, v6
	v_cvt_pk_bf16_f32 v6, v7, v8
	v_cvt_pk_bf16_f32 v7, v9, v10
	v_mul_f32_e32 v1, v112, v12
	v_permlane32_swap_b32_e32 v4, v6
	v_permlane32_swap_b32_e32 v5, v7
	global_store_dwordx4 v[2:3], v[4:7], off offset:32
	v_mul_f32_e32 v13, v113, v12
	v_mul_f32_e32 v14, v114, v12
	v_mul_f32_e32 v15, v115, v12
	v_mul_f32_e32 v16, v116, v12
	v_mul_f32_e32 v17, v117, v12
	v_mul_f32_e32 v18, v118, v12
	v_mul_f32_e32 v19, v119, v12
	v_mul_f32_e32 v1, v1, v196
	v_mul_f32_e32 v4, v13, v197
	v_mul_f32_e32 v5, v14, v198
	v_mul_f32_e32 v6, v15, v199
	v_mul_f32_e32 v7, v16, v200
	v_mul_f32_e32 v8, v17, v201
	v_mul_f32_e32 v9, v18, v202
	v_mul_f32_e32 v10, v19, v203
	v_cvt_pk_bf16_f32 v4, v1, v4
	v_cvt_pk_bf16_f32 v5, v5, v6
	v_cvt_pk_bf16_f32 v6, v7, v8
	v_cvt_pk_bf16_f32 v7, v9, v10
	v_mul_f32_e32 v1, v120, v12
	v_permlane32_swap_b32_e32 v4, v6
	v_permlane32_swap_b32_e32 v5, v7
	global_store_dwordx4 v[2:3], v[4:7], off offset:64
	v_mul_f32_e32 v13, v121, v12
	v_mul_f32_e32 v14, v122, v12
	v_mul_f32_e32 v15, v123, v12
	v_mul_f32_e32 v16, v124, v12
	v_mul_f32_e32 v17, v125, v12
	v_mul_f32_e32 v18, v126, v12
	v_mul_f32_e32 v19, v127, v12
	v_mul_f32_e32 v1, v1, v204
	v_mul_f32_e32 v4, v13, v205
	v_mul_f32_e32 v5, v14, v206
	v_mul_f32_e32 v6, v15, v207
	v_mul_f32_e32 v7, v16, v208
	v_mul_f32_e32 v8, v17, v209
	v_mul_f32_e32 v9, v18, v210
	v_mul_f32_e32 v10, v19, v211
	v_cvt_pk_bf16_f32 v4, v1, v4
	v_cvt_pk_bf16_f32 v5, v5, v6
	v_cvt_pk_bf16_f32 v6, v7, v8
	v_cvt_pk_bf16_f32 v7, v9, v10
	v_mul_f32_e32 v1, v96, v12
	v_permlane32_swap_b32_e32 v4, v6
	v_permlane32_swap_b32_e32 v5, v7
	global_store_dwordx4 v[2:3], v[4:7], off offset:96
	v_mul_f32_e32 v13, v97, v12
	v_mul_f32_e32 v14, v98, v12
	v_mul_f32_e32 v15, v99, v12
	v_mul_f32_e32 v16, v100, v12
	v_mul_f32_e32 v17, v101, v12
	v_mul_f32_e32 v18, v102, v12
	v_mul_f32_e32 v19, v103, v12
	v_mul_f32_e32 v1, v1, v212
	v_mul_f32_e32 v4, v13, v213
	v_mul_f32_e32 v5, v14, v214
	v_mul_f32_e32 v6, v15, v215
	v_mul_f32_e32 v7, v16, v216
	v_mul_f32_e32 v8, v17, v217
	v_mul_f32_e32 v9, v18, v218
	v_mul_f32_e32 v10, v19, v219
	v_cvt_pk_bf16_f32 v4, v1, v4
	v_cvt_pk_bf16_f32 v5, v5, v6
	v_cvt_pk_bf16_f32 v6, v7, v8
	v_cvt_pk_bf16_f32 v7, v9, v10
	v_mul_f32_e32 v1, v104, v12
	v_permlane32_swap_b32_e32 v4, v6
	v_permlane32_swap_b32_e32 v5, v7
	global_store_dwordx4 v[2:3], v[4:7], off offset:128
	v_mul_f32_e32 v13, v105, v12
	v_mul_f32_e32 v14, v106, v12
	v_mul_f32_e32 v15, v107, v12
	v_mul_f32_e32 v16, v108, v12
	v_mul_f32_e32 v17, v109, v12
	v_mul_f32_e32 v18, v110, v12
	v_mul_f32_e32 v19, v111, v12
	v_mul_f32_e32 v1, v1, v220
	v_mul_f32_e32 v4, v13, v221
	v_mul_f32_e32 v5, v14, v222
	v_mul_f32_e32 v6, v15, v223
	v_mul_f32_e32 v7, v16, v224
	v_mul_f32_e32 v8, v17, v225
	v_mul_f32_e32 v9, v18, v226
	v_mul_f32_e32 v10, v19, v227
	v_cvt_pk_bf16_f32 v4, v1, v4
	v_cvt_pk_bf16_f32 v5, v5, v6
	v_cvt_pk_bf16_f32 v6, v7, v8
	v_cvt_pk_bf16_f32 v7, v9, v10
	v_mul_f32_e32 v1, v80, v12
	v_permlane32_swap_b32_e32 v4, v6
	v_permlane32_swap_b32_e32 v5, v7
	global_store_dwordx4 v[2:3], v[4:7], off offset:160
	v_mul_f32_e32 v13, v81, v12
	v_mul_f32_e32 v14, v82, v12
	v_mul_f32_e32 v15, v83, v12
	v_mul_f32_e32 v16, v84, v12
	v_mul_f32_e32 v17, v85, v12
	v_mul_f32_e32 v18, v86, v12
	v_mul_f32_e32 v19, v87, v12
	v_mul_f32_e32 v1, v1, v228
	v_mul_f32_e32 v4, v13, v229
	v_mul_f32_e32 v5, v14, v230
	v_mul_f32_e32 v6, v15, v231
	v_mul_f32_e32 v7, v16, v232
	v_mul_f32_e32 v8, v17, v233
	v_mul_f32_e32 v9, v18, v234
	v_mul_f32_e32 v10, v19, v235
	v_cvt_pk_bf16_f32 v4, v1, v4
	v_cvt_pk_bf16_f32 v5, v5, v6
	v_cvt_pk_bf16_f32 v6, v7, v8
	v_cvt_pk_bf16_f32 v7, v9, v10
	v_mul_f32_e32 v1, v88, v12
	v_permlane32_swap_b32_e32 v4, v6
	v_permlane32_swap_b32_e32 v5, v7
	global_store_dwordx4 v[2:3], v[4:7], off offset:192
	v_mul_f32_e32 v13, v89, v12
	v_mul_f32_e32 v14, v90, v12
	v_mul_f32_e32 v15, v91, v12
	v_mul_f32_e32 v16, v92, v12
	v_mul_f32_e32 v17, v93, v12
	v_mul_f32_e32 v18, v94, v12
	v_mul_f32_e32 v12, v95, v12
	v_mul_f32_e32 v1, v1, v236
	v_mul_f32_e32 v4, v13, v237
	v_mul_f32_e32 v5, v14, v238
	v_mul_f32_e32 v6, v15, v239
	v_mul_f32_e32 v7, v16, v240
	v_mul_f32_e32 v8, v17, v241
	v_mul_f32_e32 v9, v18, v242
	v_mul_f32_e32 v10, v12, v243
	v_cvt_pk_bf16_f32 v4, v1, v4
	v_cvt_pk_bf16_f32 v5, v5, v6
	v_cvt_pk_bf16_f32 v6, v7, v8
	v_cvt_pk_bf16_f32 v7, v9, v10
	s_nop 0
	v_permlane32_swap_b32_e32 v4, v6
	v_permlane32_swap_b32_e32 v5, v7
	global_store_dwordx4 v[2:3], v[4:7], off offset:224
